# LDS bank conflicts: fp8 GEMM fragment reads re-mapped to the conflict-free chunk pattern (chunks fq and 4+fq, second read at +1024)
# speedup vs baseline: 1.0228x; 1.0228x over previous
; #define PG8_STAGE(bufoff, gbase, voff) do { _Pragma("unroll") for (int _i = 0; _i < 2; ++_i) \
;         __builtin_amdgcn_global_load_lds((const unsigned*)((const char*)(gbase) + (voff)[_i]), (PG8_LAS unsigned*)(lds + (bufoff) + ldsw + _i * 8192), 16, 0, 0); } while (0)
; #define PG8_WAIT_V(n) asm volatile("s_waitcnt vmcnt(" #n ")" ::: "memory")
; #define PG8_BAR __builtin_amdgcn_s_barrier()
; template <class Epi, class Sched, bool ALIGN_EPI = false, bool SP2 = false, bool GATHER = false, bool F8 = false>
; __device__ __forceinline__ void gemm_phase(PG8_LAS unsigned char* lds, const Gemm g, const Sched& S, const Epi& E) {
;     ...
;     const unsigned ldsw = (unsigned)wid * 1024u;
;     const int aoff = lds_byte(wr * 64 + fr, F8 ? fq * 16 : fq * 8), boff = lds_byte(wc * 32 + fr, F8 ? fq * 16 : fq * 8);
;     const int sc1 = 0x7f7f7f7f;
;     constexpr int KFR = F8 ? 16 : 1024;
;     ...
;     if constexpr (SP2) {
;         PG8_STAGE(PG8_SB(0, 0), cB, voffB); PG8_STAGE(PG8_SB(0, 1), cB + hstep, voffB); PG8_STAGE_A(PG8_SA(0, 0), cA, 0, false); PG8_STAGE_A(PG8_SA(0, 1), cA, 1, false);
;         if (wr == 1) PG8_BAR;
;         PG8_WAIT_V(2); PG8_BAR;
;         PG8_STAGE(PG8_SB(1, 0), cB + kstep, voffB); PG8_STAGE_A(PG8_SA(1, 0), cA + kstep, 0, false); PG8_STAGE(PG8_SB(1, 1), cB + hstep + kstep, voffB);
;         PG8_WAIT_V(6); PG8_BAR;
.LBB0_1378:
	s_add_u32 s14, s50, 0x8ac00000
	s_addc_u32 s15, s51, 0
	s_add_u32 s16, s50, 0x78c00080
	s_addc_u32 s17, s51, 0
	s_lshl_b32 s4, s4, 5
	s_mov_b64 s[18:19], 0x80
	s_and_b32 s34, s4, 0x60
	s_add_i32 m0, s29, 0x18000
	v_lshl_add_u64 v[4:5], v[4:5], 0, s[18:19]
	s_ashr_i32 s68, s93, 31
	s_lshl_b32 s7, s1, 13
	s_lshr_b32 s22, s34, 3
	s_waitcnt vmcnt(2)
	s_barrier
	global_load_lds_dwordx4 v[4:5], off
	v_lshl_add_u64 v[2:3], v[2:3], 0, s[18:19]
	s_add_i32 m0, s29, 0x1a000
	s_add_i32 s69, s29, 0x8000
	s_add_i32 s70, s29, 0xa000
	global_load_lds_dwordx4 v[2:3], off
	v_lshl_add_u64 v[2:3], s[16:17], 0, v[162:163]
	s_mov_b32 m0, s69
	s_add_u32 s4, s62, 0x40080
	global_load_lds_dwordx4 v[2:3], off
	v_lshl_add_u64 v[2:3], s[16:17], 0, v[172:173]
	s_mov_b32 m0, s70
	s_addc_u32 s5, s63, 0
	global_load_lds_dwordx4 v[2:3], off
	s_add_i32 m0, s29, 0x1c000
	v_lshl_add_u64 v[2:3], s[4:5], 0, v[164:165]
	global_load_lds_dwordx4 v[2:3], off
	v_lshl_add_u64 v[2:3], s[4:5], 0, v[166:167]
	s_add_i32 m0, s29, 0x1e000
	v_lshlrev_b32_e32 v5, 1, v0
	global_load_lds_dwordx4 v[2:3], off
	v_lshrrev_b32_e32 v2, 4, v0
	v_and_b32_e32 v3, 15, v0
	v_lshlrev_b32_e32 v8, 2, v0
	v_bfe_u32 v2, v2, 1, 1
	v_and_b32_e32 v5, 32, v5
	v_and_b32_e32 v8, 32, v8
	v_lshl_or_b32 v173, s1, 6, v3
	v_lshlrev_b32_e32 v3, 6, v3
	v_lshlrev_b32_e32 v6, 10, v2
	v_lshlrev_b32_e32 v7, 6, v0
	s_movk_i32 s4, 0x3c0
	v_bitop3_b32 v3, v3, v8, v5 bitop3:0x36
	v_or_b32_e32 v2, s22, v2
	s_cmpk_lt_u32 s0, 0x100
	v_and_or_b32 v7, v7, s4, v5
	v_or3_b32 v3, s7, v6, v3
	v_lshlrev_b32_e32 v2, 10, v2
	s_waitcnt vmcnt(6)
	s_cselect_b64 s[22:23], -1, 0
	s_ashr_i32 s7, s6, 31
	v_bfe_u32 v4, v0, 4, 2
	v_bitop3_b32 v195, v2, v7, v8 bitop3:0xf6
	v_mov_b64_e32 v[168:169], s[6:7]
	s_add_i32 s7, 0, 0x10000
	s_add_i32 s71, 0, 0x14000
	v_lshl_or_b32 v196, v4, 3, s34
	v_add_u32_e32 v197, s7, v195
	v_add_u32_e32 v198, s71, v195
	v_add_u32_e32 v199, 0, v3
	v_bfe_u32 v244, v224, 4, 1
	v_bfe_u32 v245, v224, 5, 1
	v_bfe_u32 v246, v224, 3, 1
	v_xor_b32_e32 v247, v245, v246
	v_xor_b32_e32 v246, v244, v246
	v_sub_u32_e32 v247, v247, v246
	v_lshlrev_b32_e32 v247, 5, v247
	v_lshl_add_u32 v247, v244, 4, v247
	v_lshlrev_b32_e32 v245, 10, v245
	v_sub_u32_e32 v247, v247, v245
	v_add_u32_e32 v195, v195, v247
	v_add_u32_e32 v197, v197, v247
	v_add_u32_e32 v198, v198, v247
	v_add_u32_e32 v199, v199, v247
	v_mov_b32_e32 v200, 0x7f7f7f7f
	s_mov_b64 s[34:35], 0x2000
	s_mov_b32 s72, 0xc0e00000
	s_mov_b32 s73, 0x40000
	s_mov_b32 s74, 0x48000
	s_mov_b32 s75, 0x50000
	v_mov_b32_e32 v201, 0x40e00000
	v_mov_b32_e32 v171, v162
	s_barrier
	s_branch .LBB0_1381

; #define PG8_STAGE(bufoff, gbase, voff) do { _Pragma("unroll") for (int _i = 0; _i < 2; ++_i) \
;         __builtin_amdgcn_global_load_lds((const unsigned*)((const char*)(gbase) + (voff)[_i]), (PG8_LAS unsigned*)(lds + (bufoff) + ldsw + _i * 8192), 16, 0, 0); } while (0)
; #define PG8_LDA(dst, b, h) do { _Pragma("unroll") for (int m = 0; m < 4; ++m) _Pragma("unroll") for (int k = 0; k < 2; ++k) dst[m][k] = *(const PG8_LAS bf16x8*)(lds + PG8_SA(b, h) + aoff + m * 2048 + k * KFR); } while (0)
; #define PG8_LDB(dst, b, h) do { _Pragma("unroll") for (int n = 0; n < 2; ++n) _Pragma("unroll") for (int k = 0; k < 2; ++k) dst[n][k] = *(const PG8_LAS bf16x8*)(lds + PG8_SB(b, h) + boff + n * 2048 + k * KFR); } while (0)
; #define PG8_WAIT_V(n) asm volatile("s_waitcnt vmcnt(" #n ")" ::: "memory")
; #define PG8_WAIT_L(n) asm volatile("s_waitcnt lgkmcnt(" #n ")" ::: "memory")
; #define PG8_BAR __builtin_amdgcn_s_barrier()
; #define PG8_SCHED __builtin_amdgcn_sched_barrier(0)
; template <class Epi, class Sched, bool ALIGN_EPI = false, bool SP2 = false, bool GATHER = false, bool F8 = false>
; __device__ __forceinline__ void gemm_phase(PG8_LAS unsigned char* lds, const Gemm g, const Sched& S, const Epi& E) {
;     ...
;             if constexpr (SP2) {
;             PG8_LDB(B0, 0, 0); PG8_LDB(B1, 0, 1); PG8_SCHED; PG8_LDA(At, 0, 0); PG8_STAGE_A(PG8_SA(1, 1), a1, 1, false);
;             PG8_WAIT_V(8); PG8_WAIT_L(0); PG8_BAR; PG8_MMA(0, 0, At, B0); PG8_MMA(0, 1, At, B1); PG8_BAR; PG8_SCHED;
;             PG8_LDA(At, 0, 1); PG8_STAGE(PG8_SB(0, 0), b2, voffB); PG8_STAGE(PG8_SB(0, 1), b2 + hstep, voffB); PG8_STAGE_A(PG8_SA(0, 0), a2, 0, last);
;             PG8_WAIT_V(8); PG8_WAIT_L(0); PG8_BAR; PG8_MMA(1, 0, At, B0); PG8_MMA(1, 1, At, B1); PG8_BAR; PG8_SCHED;
.LBB0_1386:
	ds_read_b128 v[26:29], v197
	ds_read_b128 v[30:33], v197 offset:1024
	ds_read_b128 v[18:21], v197 offset:2048
	ds_read_b128 v[22:25], v197 offset:3072
	ds_read_b128 v[10:13], v198
	ds_read_b128 v[14:17], v198 offset:1024
	ds_read_b128 v[2:5], v198 offset:2048
	ds_read_b128 v[6:9], v198 offset:3072
	s_add_u32 s4, s64, 0x100
	s_addc_u32 s5, s65, 0
	s_add_u32 s66, s55, s64
	s_addc_u32 s67, s76, s65
	s_cmpk_eq_i32 s64, 0x700
	s_cselect_b64 vcc, -1, 0
	s_and_b64 s[62:63], vcc, exec
	s_cselect_b32 s79, 0, s4
	s_cselect_b32 s78, 0, s5
	s_cselect_b32 s62, s53, s66
	s_cselect_b32 s63, s37, s67
	s_add_u32 s66, s8, s79
	s_addc_u32 s67, s9, s78
	v_lshl_add_u64 v[222:223], v[180:181], 0, s[64:65]
	s_add_i32 m0, s29, 0xc000
	ds_read_b128 v[182:185], v199
	ds_read_b128 v[186:189], v199 offset:1024
	ds_read_b128 v[206:209], v199 offset:2048
	ds_read_b128 v[210:213], v199 offset:3072
	ds_read_b128 v[214:217], v199 offset:4096
	ds_read_b128 v[218:221], v199 offset:5120
	ds_read_b128 v[228:231], v199 offset:6144
	ds_read_b128 v[232:235], v199 offset:7168
	global_load_lds_dwordx4 v[222:223], off
	v_lshl_add_u64 v[222:223], v[178:179], 0, s[64:65]
	s_add_i32 m0, s29, 0xe000
	s_nop 0
	global_load_lds_dwordx4 v[222:223], off
	s_waitcnt vmcnt(8)
	s_waitcnt lgkmcnt(0)
	s_barrier
	s_setprio 1
	s_waitcnt lgkmcnt(0)
	v_mfma_scale_f32_16x16x128_f8f6f4 v[158:161], v[26:33], v[182:189], v[158:161], v200, v200 op_sel_hi:[0,0,0]
	v_mfma_scale_f32_16x16x128_f8f6f4 v[154:157], v[18:25], v[182:189], v[154:157], v200, v200 op_sel_hi:[0,0,0]
	v_mfma_scale_f32_16x16x128_f8f6f4 v[142:145], v[26:33], v[206:213], v[142:145], v200, v200 op_sel_hi:[0,0,0]
	v_mfma_scale_f32_16x16x128_f8f6f4 v[134:137], v[18:25], v[206:213], v[134:137], v200, v200 op_sel_hi:[0,0,0]
	v_mfma_scale_f32_16x16x128_f8f6f4 v[126:129], v[26:33], v[214:221], v[126:129], v200, v200 op_sel_hi:[0,0,0]
	v_mfma_scale_f32_16x16x128_f8f6f4 v[118:121], v[18:25], v[214:221], v[118:121], v200, v200 op_sel_hi:[0,0,0]
	v_mfma_scale_f32_16x16x128_f8f6f4 v[110:113], v[26:33], v[228:235], v[110:113], v200, v200 op_sel_hi:[0,0,0]
	v_mfma_scale_f32_16x16x128_f8f6f4 v[102:105], v[18:25], v[228:235], v[102:105], v200, v200 op_sel_hi:[0,0,0]
	s_setprio 0
	s_setprio 1
	v_mfma_scale_f32_16x16x128_f8f6f4 v[150:153], v[10:17], v[182:189], v[150:153], v200, v200 op_sel_hi:[0,0,0]
	v_mfma_scale_f32_16x16x128_f8f6f4 v[146:149], v[2:9], v[182:189], v[146:149], v200, v200 op_sel_hi:[0,0,0]
	v_mfma_scale_f32_16x16x128_f8f6f4 v[138:141], v[10:17], v[206:213], v[138:141], v200, v200 op_sel_hi:[0,0,0]
	v_mfma_scale_f32_16x16x128_f8f6f4 v[130:133], v[2:9], v[206:213], v[130:133], v200, v200 op_sel_hi:[0,0,0]
	v_mfma_scale_f32_16x16x128_f8f6f4 v[122:125], v[10:17], v[214:221], v[122:125], v200, v200 op_sel_hi:[0,0,0]
	v_mfma_scale_f32_16x16x128_f8f6f4 v[114:117], v[2:9], v[214:221], v[114:117], v200, v200 op_sel_hi:[0,0,0]
	v_mfma_scale_f32_16x16x128_f8f6f4 v[106:109], v[10:17], v[228:235], v[106:109], v200, v200 op_sel_hi:[0,0,0]
	v_mfma_scale_f32_16x16x128_f8f6f4 v[98:101], v[2:9], v[228:235], v[98:101], v200, v200 op_sel_hi:[0,0,0]
	s_setprio 0
	s_barrier
	s_add_i32 s64, s7, s25
	v_lshl_add_u64 v[182:183], s[62:63], 0, v[164:165]
	s_mov_b32 m0, s64
	ds_read_b128 v[206:209], v199 offset:16384
	ds_read_b128 v[210:213], v199 offset:17408
	ds_read_b128 v[214:217], v199 offset:18432
	ds_read_b128 v[218:221], v199 offset:19456
	ds_read_b128 v[228:231], v199 offset:20480
	ds_read_b128 v[232:235], v199 offset:21504
	ds_read_b128 v[236:239], v199 offset:22528
	ds_read_b128 v[240:243], v199 offset:23552
	global_load_lds_dwordx4 v[182:183], off
	s_add_i32 m0, s64, 0x2000
	s_add_u32 s64, s62, 0x40000
	v_lshl_add_u64 v[184:185], s[62:63], 0, v[166:167]
	s_addc_u32 s65, s63, 0
	s_add_i32 s78, s71, s25
	global_load_lds_dwordx4 v[184:185], off
	v_lshl_add_u64 v[186:187], s[64:65], 0, v[164:165]
	s_mov_b32 m0, s78
	v_cndmask_b32_e32 v162, v171, v202, vcc
	global_load_lds_dwordx4 v[186:187], off
	v_lshl_add_u64 v[186:187], s[64:65], 0, v[166:167]
	s_add_i32 m0, s78, 0x2000
	s_nop 0
	global_load_lds_dwordx4 v[186:187], off
	s_mov_b32 m0, s29
	v_lshl_add_u64 v[186:187], s[66:67], 0, v[162:163]
	global_load_lds_dwordx4 v162, s[66:67]
	v_cndmask_b32_e32 v162, v172, v204, vcc
	s_mov_b32 m0, s30
	v_lshl_add_u64 v[188:189], s[66:67], 0, v[162:163]
	global_load_lds_dwordx4 v162, s[66:67]
	s_waitcnt vmcnt(8)
	s_waitcnt lgkmcnt(0)
	s_barrier
	s_setprio 1
	s_waitcnt lgkmcnt(0)
	v_mfma_scale_f32_16x16x128_f8f6f4 v[94:97], v[26:33], v[206:213], v[94:97], v200, v200 op_sel_hi:[0,0,0]
	v_mfma_scale_f32_16x16x128_f8f6f4 v[86:89], v[18:25], v[206:213], v[86:89], v200, v200 op_sel_hi:[0,0,0]
	v_mfma_scale_f32_16x16x128_f8f6f4 v[78:81], v[26:33], v[214:221], v[78:81], v200, v200 op_sel_hi:[0,0,0]
	v_mfma_scale_f32_16x16x128_f8f6f4 v[70:73], v[18:25], v[214:221], v[70:73], v200, v200 op_sel_hi:[0,0,0]
	v_mfma_scale_f32_16x16x128_f8f6f4 v[62:65], v[26:33], v[228:235], v[62:65], v200, v200 op_sel_hi:[0,0,0]
	v_mfma_scale_f32_16x16x128_f8f6f4 v[54:57], v[18:25], v[228:235], v[54:57], v200, v200 op_sel_hi:[0,0,0]
	v_mfma_scale_f32_16x16x128_f8f6f4 v[46:49], v[26:33], v[236:243], v[46:49], v200, v200 op_sel_hi:[0,0,0]
	v_mfma_scale_f32_16x16x128_f8f6f4 v[38:41], v[18:25], v[236:243], v[38:41], v200, v200 op_sel_hi:[0,0,0]
	s_setprio 0
	s_setprio 1
	v_mfma_scale_f32_16x16x128_f8f6f4 v[90:93], v[10:17], v[206:213], v[90:93], v200, v200 op_sel_hi:[0,0,0]
	v_mfma_scale_f32_16x16x128_f8f6f4 v[82:85], v[2:9], v[206:213], v[82:85], v200, v200 op_sel_hi:[0,0,0]
	v_mfma_scale_f32_16x16x128_f8f6f4 v[74:77], v[10:17], v[214:221], v[74:77], v200, v200 op_sel_hi:[0,0,0]
	v_mfma_scale_f32_16x16x128_f8f6f4 v[66:69], v[2:9], v[214:221], v[66:69], v200, v200 op_sel_hi:[0,0,0]
	v_mfma_scale_f32_16x16x128_f8f6f4 v[58:61], v[10:17], v[228:235], v[58:61], v200, v200 op_sel_hi:[0,0,0]
	v_mfma_scale_f32_16x16x128_f8f6f4 v[50:53], v[2:9], v[228:235], v[50:53], v200, v200 op_sel_hi:[0,0,0]
	v_mfma_scale_f32_16x16x128_f8f6f4 v[42:45], v[10:17], v[236:243], v[42:45], v200, v200 op_sel_hi:[0,0,0]
	v_mfma_scale_f32_16x16x128_f8f6f4 v[34:37], v[2:9], v[236:243], v[34:37], v200, v200 op_sel_hi:[0,0,0]
	s_setprio 0
	s_barrier
; #define PG8_STAGE(bufoff, gbase, voff) do { _Pragma("unroll") for (int _i = 0; _i < 2; ++_i) \
;         __builtin_amdgcn_global_load_lds((const unsigned*)((const char*)(gbase) + (voff)[_i]), (PG8_LAS unsigned*)(lds + (bufoff) + ldsw + _i * 8192), 16, 0, 0); } while (0)
; #define PG8_LDA(dst, b, h) do { _Pragma("unroll") for (int m = 0; m < 4; ++m) _Pragma("unroll") for (int k = 0; k < 2; ++k) dst[m][k] = *(const PG8_LAS bf16x8*)(lds + PG8_SA(b, h) + aoff + m * 2048 + k * KFR); } while (0)
; #define PG8_LDB(dst, b, h) do { _Pragma("unroll") for (int n = 0; n < 2; ++n) _Pragma("unroll") for (int k = 0; k < 2; ++k) dst[n][k] = *(const PG8_LAS bf16x8*)(lds + PG8_SB(b, h) + boff + n * 2048 + k * KFR); } while (0)
; #define PG8_WAIT_V(n) asm volatile("s_waitcnt vmcnt(" #n ")" ::: "memory")
; #define PG8_WAIT_L(n) asm volatile("s_waitcnt lgkmcnt(" #n ")" ::: "memory")
; #define PG8_BAR __builtin_amdgcn_s_barrier()
; #define PG8_SCHED __builtin_amdgcn_sched_barrier(0)
; template <class Epi, class Sched, bool ALIGN_EPI = false, bool SP2 = false, bool GATHER = false, bool F8 = false>
; __device__ __forceinline__ void gemm_phase(PG8_LAS unsigned char* lds, const Gemm g, const Sched& S, const Epi& E) {
;     ...
;             PG8_LDB(B0, 1, 0); PG8_LDB(B1, 1, 1); PG8_SCHED; PG8_LDA(At, 1, 0); PG8_STAGE_A(PG8_SA(0, 1), a2, 1, last);
;             PG8_WAIT_V(8); PG8_WAIT_L(0); PG8_BAR; PG8_MMA(0, 0, At, B0); PG8_MMA(0, 1, At, B1); PG8_BAR; PG8_SCHED;
;             PG8_LDA(At, 1, 1); PG8_STAGE(PG8_SB(1, 0), b3, voffB); PG8_STAGE(PG8_SB(1, 1), b3 + hstep, voffB); PG8_STAGE_A(PG8_SA(1, 0), a3, 0, last);
;             PG8_WAIT_V(8); PG8_WAIT_L(0); PG8_BAR; PG8_MMA(1, 0, At, B0); PG8_MMA(1, 1, At, B1); PG8_BAR; PG8_SCHED;
	s_add_i32 s64, 0, 0x18000
	s_add_i32 s65, 0, 0x1c000
	v_add_u32_e32 v14, s64, v195
	v_add_u32_e32 v30, s65, v195
	ds_read_b128 v[2:5], v14
	ds_read_b128 v[6:9], v14 offset:1024
	ds_read_b128 v[10:13], v14 offset:2048
	ds_read_b128 v[14:17], v14 offset:3072
	ds_read_b128 v[18:21], v30
	ds_read_b128 v[22:25], v30 offset:1024
	ds_read_b128 v[26:29], v30 offset:2048
	ds_read_b128 v[30:33], v30 offset:3072
	s_mov_b32 m0, s31
	v_cndmask_b32_e32 v162, v174, v203, vcc
	ds_read_b128 v[206:209], v199 offset:32768
	ds_read_b128 v[210:213], v199 offset:33792
	ds_read_b128 v[214:217], v199 offset:34816
	ds_read_b128 v[218:221], v199 offset:35840
	ds_read_b128 v[228:231], v199 offset:36864
	ds_read_b128 v[232:235], v199 offset:37888
	ds_read_b128 v[236:239], v199 offset:38912
	ds_read_b128 v[240:243], v199 offset:39936
	global_load_lds_dwordx4 v162, s[66:67]
	v_cndmask_b32_e32 v162, v176, v205, vcc
	s_mov_b32 m0, s33
	s_nop 0
	global_load_lds_dwordx4 v162, s[66:67]
	s_waitcnt vmcnt(8)
	s_waitcnt lgkmcnt(0)
	s_barrier
	s_setprio 1
	s_waitcnt lgkmcnt(0)
	v_mfma_scale_f32_16x16x128_f8f6f4 v[158:161], v[2:9], v[206:213], v[158:161], v200, v200 op_sel_hi:[0,0,0]
	v_mfma_scale_f32_16x16x128_f8f6f4 v[154:157], v[10:17], v[206:213], v[154:157], v200, v200 op_sel_hi:[0,0,0]
	v_mfma_scale_f32_16x16x128_f8f6f4 v[142:145], v[2:9], v[214:221], v[142:145], v200, v200 op_sel_hi:[0,0,0]
	v_mfma_scale_f32_16x16x128_f8f6f4 v[134:137], v[10:17], v[214:221], v[134:137], v200, v200 op_sel_hi:[0,0,0]
	v_mfma_scale_f32_16x16x128_f8f6f4 v[126:129], v[2:9], v[228:235], v[126:129], v200, v200 op_sel_hi:[0,0,0]
	v_mfma_scale_f32_16x16x128_f8f6f4 v[118:121], v[10:17], v[228:235], v[118:121], v200, v200 op_sel_hi:[0,0,0]
	v_mfma_scale_f32_16x16x128_f8f6f4 v[110:113], v[2:9], v[236:243], v[110:113], v200, v200 op_sel_hi:[0,0,0]
	v_mfma_scale_f32_16x16x128_f8f6f4 v[102:105], v[10:17], v[236:243], v[102:105], v200, v200 op_sel_hi:[0,0,0]
	s_setprio 0
	s_setprio 1
	v_mfma_scale_f32_16x16x128_f8f6f4 v[150:153], v[18:25], v[206:213], v[150:153], v200, v200 op_sel_hi:[0,0,0]
	v_mfma_scale_f32_16x16x128_f8f6f4 v[146:149], v[26:33], v[206:213], v[146:149], v200, v200 op_sel_hi:[0,0,0]
	v_mfma_scale_f32_16x16x128_f8f6f4 v[138:141], v[18:25], v[214:221], v[138:141], v200, v200 op_sel_hi:[0,0,0]
	v_mfma_scale_f32_16x16x128_f8f6f4 v[130:133], v[26:33], v[214:221], v[130:133], v200, v200 op_sel_hi:[0,0,0]
	v_mfma_scale_f32_16x16x128_f8f6f4 v[122:125], v[18:25], v[228:235], v[122:125], v200, v200 op_sel_hi:[0,0,0]
	v_mfma_scale_f32_16x16x128_f8f6f4 v[114:117], v[26:33], v[228:235], v[114:117], v200, v200 op_sel_hi:[0,0,0]
	v_mfma_scale_f32_16x16x128_f8f6f4 v[106:109], v[18:25], v[236:243], v[106:109], v200, v200 op_sel_hi:[0,0,0]
	v_mfma_scale_f32_16x16x128_f8f6f4 v[98:101], v[26:33], v[236:243], v[98:101], v200, v200 op_sel_hi:[0,0,0]
	s_setprio 0
	s_barrier
	s_add_i32 s64, s64, s25
	v_lshl_add_u64 v[182:183], v[182:183], 0, s[18:19]
	s_mov_b32 m0, s64
	ds_read_b128 v[206:209], v199 offset:49152
	ds_read_b128 v[210:213], v199 offset:50176
	ds_read_b128 v[214:217], v199 offset:51200
	ds_read_b128 v[218:221], v199 offset:52224
	ds_read_b128 v[228:231], v199 offset:53248
	ds_read_b128 v[232:235], v199 offset:54272
	ds_read_b128 v[236:239], v199 offset:55296
	ds_read_b128 v[240:243], v199 offset:56320
	global_load_lds_dwordx4 v[182:183], off
	s_add_i32 m0, s64, 0x2000
	s_add_u32 s62, s62, 0x40080
	v_lshl_add_u64 v[182:183], v[184:185], 0, s[18:19]
	s_addc_u32 s63, s63, 0
	s_add_i32 s64, s65, s25
	global_load_lds_dwordx4 v[182:183], off
	v_lshl_add_u64 v[182:183], s[62:63], 0, v[164:165]
	s_mov_b32 m0, s64
	s_nop 0
	global_load_lds_dwordx4 v[182:183], off
	v_lshl_add_u64 v[182:183], s[62:63], 0, v[166:167]
	s_add_i32 m0, s64, 0x2000
	s_nop 0
	global_load_lds_dwordx4 v[182:183], off
	v_lshl_add_u64 v[182:183], v[186:187], 0, s[18:19]
	s_mov_b32 m0, s69
	s_nop 0
	global_load_lds_dwordx4 v[182:183], off
	v_lshl_add_u64 v[182:183], v[188:189], 0, s[18:19]
	s_mov_b32 m0, s70
	s_nop 0
	global_load_lds_dwordx4 v[182:183], off
	s_waitcnt vmcnt(8)
	v_lshl_or_b32 v202, v248, 11, v192
	v_lshl_or_b32 v203, v249, 11, v192
	v_lshl_or_b32 v204, v250, 11, v193
	v_lshl_or_b32 v205, v251, 11, v193
	s_waitcnt lgkmcnt(0)
	s_barrier
	s_setprio 1
	s_waitcnt lgkmcnt(0)
	v_mfma_scale_f32_16x16x128_f8f6f4 v[94:97], v[2:9], v[206:213], v[94:97], v200, v200 op_sel_hi:[0,0,0]
	v_mfma_scale_f32_16x16x128_f8f6f4 v[86:89], v[10:17], v[206:213], v[86:89], v200, v200 op_sel_hi:[0,0,0]
	v_mfma_scale_f32_16x16x128_f8f6f4 v[78:81], v[2:9], v[214:221], v[78:81], v200, v200 op_sel_hi:[0,0,0]
	v_mfma_scale_f32_16x16x128_f8f6f4 v[70:73], v[10:17], v[214:221], v[70:73], v200, v200 op_sel_hi:[0,0,0]
	v_mfma_scale_f32_16x16x128_f8f6f4 v[62:65], v[2:9], v[228:235], v[62:65], v200, v200 op_sel_hi:[0,0,0]
	v_mfma_scale_f32_16x16x128_f8f6f4 v[54:57], v[10:17], v[228:235], v[54:57], v200, v200 op_sel_hi:[0,0,0]
	v_mfma_scale_f32_16x16x128_f8f6f4 v[46:49], v[2:9], v[236:243], v[46:49], v200, v200 op_sel_hi:[0,0,0]
	v_mfma_scale_f32_16x16x128_f8f6f4 v[38:41], v[10:17], v[236:243], v[38:41], v200, v200 op_sel_hi:[0,0,0]
	s_setprio 0
	s_setprio 1
	v_mfma_scale_f32_16x16x128_f8f6f4 v[90:93], v[18:25], v[206:213], v[90:93], v200, v200 op_sel_hi:[0,0,0]
	v_mfma_scale_f32_16x16x128_f8f6f4 v[82:85], v[26:33], v[206:213], v[82:85], v200, v200 op_sel_hi:[0,0,0]
	v_mfma_scale_f32_16x16x128_f8f6f4 v[74:77], v[18:25], v[214:221], v[74:77], v200, v200 op_sel_hi:[0,0,0]
	v_mfma_scale_f32_16x16x128_f8f6f4 v[66:69], v[26:33], v[214:221], v[66:69], v200, v200 op_sel_hi:[0,0,0]
	v_mfma_scale_f32_16x16x128_f8f6f4 v[58:61], v[18:25], v[228:235], v[58:61], v200, v200 op_sel_hi:[0,0,0]
	v_mfma_scale_f32_16x16x128_f8f6f4 v[50:53], v[26:33], v[228:235], v[50:53], v200, v200 op_sel_hi:[0,0,0]
	v_mfma_scale_f32_16x16x128_f8f6f4 v[42:45], v[18:25], v[236:243], v[42:45], v200, v200 op_sel_hi:[0,0,0]
	v_mfma_scale_f32_16x16x128_f8f6f4 v[34:37], v[26:33], v[236:243], v[34:37], v200, v200 op_sel_hi:[0,0,0]
	s_setprio 0
	s_barrier
	s_add_i32 s77, s77, 2
	s_cmp_gt_u32 s77, 13
	s_mov_b64 s[64:65], s[4:5]
	s_cbranch_scc0 .LBB0_1386
	s_and_b64 vcc, exec, s[22:23]
	s_cbranch_vccz .LBB0_1389
	s_barrier

; #define PG8_STAGE(bufoff, gbase, voff) do { _Pragma("unroll") for (int _i = 0; _i < 2; ++_i) \
;         __builtin_amdgcn_global_load_lds((const unsigned*)((const char*)(gbase) + (voff)[_i]), (PG8_LAS unsigned*)(lds + (bufoff) + ldsw + _i * 8192), 16, 0, 0); } while (0)
; #define PG8_WAIT_V(n) asm volatile("s_waitcnt vmcnt(" #n ")" ::: "memory")
; #define PG8_BAR __builtin_amdgcn_s_barrier()
; template <class Epi, class Sched, bool ALIGN_EPI = false, bool SP2 = false, bool GATHER = false, bool F8 = false>
; __device__ __forceinline__ void gemm_phase(PG8_LAS unsigned char* lds, const Gemm g, const Sched& S, const Epi& E) {
;     ...
;     const unsigned ldsw = (unsigned)wid * 1024u;
;     const int aoff = lds_byte(wr * 64 + fr, F8 ? fq * 16 : fq * 8), boff = lds_byte(wc * 32 + fr, F8 ? fq * 16 : fq * 8);
;     const int sc1 = 0x7f7f7f7f;
;     constexpr int KFR = F8 ? 16 : 1024;
;     ...
;     if constexpr (SP2) {
;         PG8_STAGE(PG8_SB(0, 0), cB, voffB); PG8_STAGE(PG8_SB(0, 1), cB + hstep, voffB); PG8_STAGE_A(PG8_SA(0, 0), cA, 0, false); PG8_STAGE_A(PG8_SA(0, 1), cA, 1, false);
;         if (wr == 1) PG8_BAR;
;         PG8_WAIT_V(2); PG8_BAR;
;         PG8_STAGE(PG8_SB(1, 0), cB + kstep, voffB); PG8_STAGE_A(PG8_SA(1, 0), cA + kstep, 0, false); PG8_STAGE(PG8_SB(1, 1), cB + hstep + kstep, voffB);
;         PG8_WAIT_V(6); PG8_BAR;
.LBB0_1557:
	s_add_u32 s8, s50, 0x9cc00000
	s_addc_u32 s9, s51, 0
	s_add_u32 s10, s50, 0xb00000
	s_addc_u32 s11, s51, 0
	s_lshl_b32 s12, s12, 5
	s_and_b32 s22, s12, 0x60
	s_mov_b64 s[12:13], 0x80
	s_add_i32 m0, s29, 0x18000
	v_lshl_add_u64 v[8:9], v[8:9], 0, s[12:13]
	s_ashr_i32 s57, s93, 31
	s_lshl_b32 s16, s1, 13
	s_lshr_b32 s18, s22, 3
	s_waitcnt vmcnt(2)
	s_barrier
	global_load_lds_dwordx4 v[8:9], off
	v_lshl_add_u64 v[6:7], v[6:7], 0, s[12:13]
	s_add_i32 m0, s29, 0x1a000
	s_add_i32 s66, s29, 0x8000
	s_add_i32 s67, s29, 0xa000
	global_load_lds_dwordx4 v[6:7], off
	v_lshl_add_u64 v[2:3], v[2:3], 0, s[12:13]
	s_mov_b32 m0, s66
	s_add_u32 s14, s58, 0x40080
	global_load_lds_dwordx4 v[2:3], off
	v_lshl_add_u64 v[2:3], v[4:5], 0, s[12:13]
	s_mov_b32 m0, s67
	s_addc_u32 s15, s59, 0
	global_load_lds_dwordx4 v[2:3], off
	s_add_i32 m0, s29, 0x1c000
	v_lshl_add_u64 v[2:3], s[14:15], 0, v[162:163]
	global_load_lds_dwordx4 v[2:3], off
	v_lshl_add_u64 v[2:3], s[14:15], 0, v[168:169]
	s_add_i32 m0, s29, 0x1e000
	v_bfe_u32 v4, v0, 4, 2
	global_load_lds_dwordx4 v[2:3], off
	v_lshrrev_b32_e32 v2, 4, v0
	v_and_b32_e32 v3, 15, v0
	v_lshlrev_b32_e32 v5, 1, v0
	v_bfe_u32 v2, v2, 1, 1
	v_lshlrev_b32_e32 v7, 6, v0
	v_lshlrev_b32_e32 v8, 2, v0
	v_lshlrev_b32_e32 v0, 8, v0
	v_and_b32_e32 v5, 32, v5
	v_lshlrev_b32_e32 v6, 10, v2
	s_movk_i32 s14, 0x3c0
	v_or_b32_e32 v2, s18, v2
	v_lshl_or_b32 v186, v4, 3, s22
	v_and_b32_e32 v0, 0x18000, v0
	v_lshlrev_b32_e32 v4, 11, v10
	v_and_or_b32 v7, v7, s14, v5
	v_and_b32_e32 v8, 32, v8
	v_lshlrev_b32_e32 v2, 10, v2
	v_or3_b32 v0, v11, v0, v4
	v_bitop3_b32 v185, v2, v7, v8 bitop3:0xf6
	v_add_u32_e32 v2, v0, v1
	v_lshlrev_b32_e32 v0, 4, v12
	v_lshl_or_b32 v184, s1, 6, v3
	v_lshlrev_b32_e32 v3, 6, v3
	v_and_b32_e32 v0, 0x38000, v0
	v_bitop3_b32 v3, v3, v8, v5 bitop3:0x36
	s_waitcnt vmcnt(6)
	s_cmpk_lt_u32 s0, 0x100
	v_or3_b32 v0, v11, v0, v4
	v_or3_b32 v5, s16, v6, v3
	s_mov_b64 s[18:19], 0x40080
	s_cselect_b64 s[14:15], -1, 0
	v_mov_b32_e32 v3, v163
	v_add_u32_e32 v0, v0, v1
	v_mov_b32_e32 v1, v163
	s_add_i32 s68, 0, 0x10000
	s_add_i32 s69, 0, 0x14000
	v_ashrrev_i32_e32 v161, 31, v160
	v_lshl_add_u64 v[170:171], v[2:3], 0, s[18:19]
	v_lshl_add_u64 v[172:173], v[0:1], 0, s[18:19]
	v_add_u32_e32 v187, s68, v185
	v_add_u32_e32 v188, s69, v185
	v_add_u32_e32 v189, 0, v5
	v_bfe_u32 v244, v224, 4, 1
	v_bfe_u32 v245, v224, 5, 1
	v_bfe_u32 v246, v224, 3, 1
	v_xor_b32_e32 v247, v245, v246
	v_xor_b32_e32 v246, v244, v246
	v_sub_u32_e32 v247, v247, v246
	v_lshlrev_b32_e32 v247, 5, v247
	v_lshl_add_u32 v247, v244, 4, v247
	v_lshlrev_b32_e32 v245, 10, v245
	v_sub_u32_e32 v247, v247, v245
	v_add_u32_e32 v185, v185, v247
	v_add_u32_e32 v187, v187, v247
	v_add_u32_e32 v188, v188, v247
	v_add_u32_e32 v189, v189, v247
	v_mov_b32_e32 v190, 0x7f7f7f7f
	s_mov_b32 s16, 0x3b800000
	s_mov_b32 s70, 0xc3e00000
	s_mov_b32 s71, 0x40000
	s_mov_b64 s[18:19], 0x48000
	s_mov_b32 s72, 0x48000
	s_mov_b64 s[22:23], 0x50000
	s_mov_b32 s73, 0x50000
	s_mov_b64 s[34:35], 0x58000
	s_mov_b32 s74, 0x58000
	v_mov_b32_e32 v191, 0x43e00000
	s_barrier
	s_branch .LBB0_1560

; #define PG8_STAGE(bufoff, gbase, voff) do { _Pragma("unroll") for (int _i = 0; _i < 2; ++_i) \
;         __builtin_amdgcn_global_load_lds((const unsigned*)((const char*)(gbase) + (voff)[_i]), (PG8_LAS unsigned*)(lds + (bufoff) + ldsw + _i * 8192), 16, 0, 0); } while (0)
; #define PG8_LDA(dst, b, h) do { _Pragma("unroll") for (int m = 0; m < 4; ++m) _Pragma("unroll") for (int k = 0; k < 2; ++k) dst[m][k] = *(const PG8_LAS bf16x8*)(lds + PG8_SA(b, h) + aoff + m * 2048 + k * KFR); } while (0)
; #define PG8_LDB(dst, b, h) do { _Pragma("unroll") for (int n = 0; n < 2; ++n) _Pragma("unroll") for (int k = 0; k < 2; ++k) dst[n][k] = *(const PG8_LAS bf16x8*)(lds + PG8_SB(b, h) + boff + n * 2048 + k * KFR); } while (0)
; #define PG8_WAIT_V(n) asm volatile("s_waitcnt vmcnt(" #n ")" ::: "memory")
; #define PG8_WAIT_L(n) asm volatile("s_waitcnt lgkmcnt(" #n ")" ::: "memory")
; #define PG8_BAR __builtin_amdgcn_s_barrier()
; #define PG8_SCHED __builtin_amdgcn_sched_barrier(0)
; template <class Epi, class Sched, bool ALIGN_EPI = false, bool SP2 = false, bool GATHER = false, bool F8 = false>
; __device__ __forceinline__ void gemm_phase(PG8_LAS unsigned char* lds, const Gemm g, const Sched& S, const Epi& E) {
;     ...
;             if constexpr (SP2) {
;             PG8_LDB(B0, 0, 0); PG8_LDB(B1, 0, 1); PG8_SCHED; PG8_LDA(At, 0, 0); PG8_STAGE_A(PG8_SA(1, 1), a1, 1, false);
;             PG8_WAIT_V(8); PG8_WAIT_L(0); PG8_BAR; PG8_MMA(0, 0, At, B0); PG8_MMA(0, 1, At, B1); PG8_BAR; PG8_SCHED;
;             PG8_LDA(At, 0, 1); PG8_STAGE(PG8_SB(0, 0), b2, voffB); PG8_STAGE(PG8_SB(0, 1), b2 + hstep, voffB); PG8_STAGE_A(PG8_SA(0, 0), a2, 0, last);
;             PG8_WAIT_V(8); PG8_WAIT_L(0); PG8_BAR; PG8_MMA(1, 0, At, B0); PG8_MMA(1, 1, At, B1); PG8_BAR; PG8_SCHED;
.LBB0_1565:
	ds_read_b128 v[24:27], v187
	ds_read_b128 v[28:31], v187 offset:1024
	ds_read_b128 v[16:19], v187 offset:2048
	ds_read_b128 v[20:23], v187 offset:3072
	ds_read_b128 v[8:11], v188
	ds_read_b128 v[12:15], v188 offset:1024
	ds_read_b128 v[0:3], v188 offset:2048
	ds_read_b128 v[4:7], v188 offset:3072
	s_add_u32 s58, s60, 0x100
	s_addc_u32 s59, s61, 0
	s_cmp_eq_u32 s78, 12
	s_cselect_b32 s65, s39, s59
	s_cselect_b32 s64, s75, s58
	s_cselect_b32 s63, s37, s77
	s_cselect_b32 s62, s41, s76
	v_lshl_add_u64 v[216:217], s[60:61], 0, v[170:171]
	s_add_i32 m0, s29, 0xc000
	ds_read_b128 v[176:179], v189
	ds_read_b128 v[180:183], v189 offset:1024
	ds_read_b128 v[192:195], v189 offset:2048
	ds_read_b128 v[196:199], v189 offset:3072
	ds_read_b128 v[200:203], v189 offset:4096
	ds_read_b128 v[204:207], v189 offset:5120
	ds_read_b128 v[208:211], v189 offset:6144
	ds_read_b128 v[212:215], v189 offset:7168
	global_load_lds_dwordx4 v[216:217], off
	v_lshl_add_u64 v[216:217], s[60:61], 0, v[172:173]
	s_add_i32 m0, s29, 0xe000
	s_nop 0
	global_load_lds_dwordx4 v[216:217], off
	s_waitcnt vmcnt(8)
	s_waitcnt lgkmcnt(0)
	s_barrier
	s_setprio 1
	s_waitcnt lgkmcnt(0)
	v_mfma_scale_f32_16x16x128_f8f6f4 v[156:159], v[24:31], v[176:183], v[156:159], v190, v190 op_sel_hi:[0,0,0]
	v_mfma_scale_f32_16x16x128_f8f6f4 v[152:155], v[16:23], v[176:183], v[152:155], v190, v190 op_sel_hi:[0,0,0]
	v_mfma_scale_f32_16x16x128_f8f6f4 v[148:151], v[24:31], v[192:199], v[148:151], v190, v190 op_sel_hi:[0,0,0]
	v_mfma_scale_f32_16x16x128_f8f6f4 v[144:147], v[16:23], v[192:199], v[144:147], v190, v190 op_sel_hi:[0,0,0]
	v_mfma_scale_f32_16x16x128_f8f6f4 v[124:127], v[24:31], v[200:207], v[124:127], v190, v190 op_sel_hi:[0,0,0]
	v_mfma_scale_f32_16x16x128_f8f6f4 v[120:123], v[16:23], v[200:207], v[120:123], v190, v190 op_sel_hi:[0,0,0]
	v_mfma_scale_f32_16x16x128_f8f6f4 v[108:111], v[24:31], v[208:215], v[108:111], v190, v190 op_sel_hi:[0,0,0]
	v_mfma_scale_f32_16x16x128_f8f6f4 v[104:107], v[16:23], v[208:215], v[104:107], v190, v190 op_sel_hi:[0,0,0]
	s_setprio 0
	s_setprio 1
	v_mfma_scale_f32_16x16x128_f8f6f4 v[140:143], v[8:15], v[176:183], v[140:143], v190, v190 op_sel_hi:[0,0,0]
	v_mfma_scale_f32_16x16x128_f8f6f4 v[136:139], v[0:7], v[176:183], v[136:139], v190, v190 op_sel_hi:[0,0,0]
	v_mfma_scale_f32_16x16x128_f8f6f4 v[132:135], v[8:15], v[192:199], v[132:135], v190, v190 op_sel_hi:[0,0,0]
	v_mfma_scale_f32_16x16x128_f8f6f4 v[128:131], v[0:7], v[192:199], v[128:131], v190, v190 op_sel_hi:[0,0,0]
	v_mfma_scale_f32_16x16x128_f8f6f4 v[116:119], v[8:15], v[200:207], v[116:119], v190, v190 op_sel_hi:[0,0,0]
	v_mfma_scale_f32_16x16x128_f8f6f4 v[112:115], v[0:7], v[200:207], v[112:115], v190, v190 op_sel_hi:[0,0,0]
	v_mfma_scale_f32_16x16x128_f8f6f4 v[100:103], v[8:15], v[208:215], v[100:103], v190, v190 op_sel_hi:[0,0,0]
	v_mfma_scale_f32_16x16x128_f8f6f4 v[96:99], v[0:7], v[208:215], v[96:99], v190, v190 op_sel_hi:[0,0,0]
	s_setprio 0
	s_barrier
	s_add_i32 s60, s68, s26
	v_lshl_add_u64 v[176:177], s[62:63], 0, v[162:163]
	s_mov_b32 m0, s60
	ds_read_b128 v[192:195], v189 offset:16384
	ds_read_b128 v[196:199], v189 offset:17408
	ds_read_b128 v[200:203], v189 offset:18432
	ds_read_b128 v[204:207], v189 offset:19456
	ds_read_b128 v[208:211], v189 offset:20480
	ds_read_b128 v[212:215], v189 offset:21504
	ds_read_b128 v[216:219], v189 offset:22528
	ds_read_b128 v[220:223], v189 offset:23552
	global_load_lds_dwordx4 v[176:177], off
	s_add_i32 m0, s60, 0x2000
	s_add_u32 s60, s62, 0x40000
	v_lshl_add_u64 v[178:179], s[62:63], 0, v[168:169]
	s_addc_u32 s61, s63, 0
	s_add_i32 s79, s69, s26
	global_load_lds_dwordx4 v[178:179], off
	v_lshl_add_u64 v[180:181], s[60:61], 0, v[162:163]
	s_mov_b32 m0, s79
	v_lshl_add_u64 v[182:183], s[64:65], 0, v[166:167]
	global_load_lds_dwordx4 v[180:181], off
	v_lshl_add_u64 v[180:181], s[60:61], 0, v[168:169]
	s_add_i32 m0, s79, 0x2000
	s_nop 0
	global_load_lds_dwordx4 v[180:181], off
	v_lshl_add_u64 v[180:181], s[64:65], 0, v[164:165]
	s_mov_b32 m0, s29
	s_nop 0
	global_load_lds_dwordx4 v[180:181], off
	s_mov_b32 m0, s30
	s_nop 0
	global_load_lds_dwordx4 v[182:183], off
	s_waitcnt vmcnt(8)
	s_waitcnt lgkmcnt(0)
	s_barrier
	s_setprio 1
	s_waitcnt lgkmcnt(0)
	v_mfma_scale_f32_16x16x128_f8f6f4 v[92:95], v[24:31], v[192:199], v[92:95], v190, v190 op_sel_hi:[0,0,0]
	v_mfma_scale_f32_16x16x128_f8f6f4 v[88:91], v[16:23], v[192:199], v[88:91], v190, v190 op_sel_hi:[0,0,0]
	v_mfma_scale_f32_16x16x128_f8f6f4 v[76:79], v[24:31], v[200:207], v[76:79], v190, v190 op_sel_hi:[0,0,0]
	v_mfma_scale_f32_16x16x128_f8f6f4 v[72:75], v[16:23], v[200:207], v[72:75], v190, v190 op_sel_hi:[0,0,0]
	v_mfma_scale_f32_16x16x128_f8f6f4 v[60:63], v[24:31], v[208:215], v[60:63], v190, v190 op_sel_hi:[0,0,0]
	v_mfma_scale_f32_16x16x128_f8f6f4 v[56:59], v[16:23], v[208:215], v[56:59], v190, v190 op_sel_hi:[0,0,0]
	v_mfma_scale_f32_16x16x128_f8f6f4 v[44:47], v[24:31], v[216:223], v[44:47], v190, v190 op_sel_hi:[0,0,0]
	v_mfma_scale_f32_16x16x128_f8f6f4 v[40:43], v[16:23], v[216:223], v[40:43], v190, v190 op_sel_hi:[0,0,0]
	s_setprio 0
	s_setprio 1
	v_mfma_scale_f32_16x16x128_f8f6f4 v[84:87], v[8:15], v[192:199], v[84:87], v190, v190 op_sel_hi:[0,0,0]
	v_mfma_scale_f32_16x16x128_f8f6f4 v[80:83], v[0:7], v[192:199], v[80:83], v190, v190 op_sel_hi:[0,0,0]
	v_mfma_scale_f32_16x16x128_f8f6f4 v[68:71], v[8:15], v[200:207], v[68:71], v190, v190 op_sel_hi:[0,0,0]
	v_mfma_scale_f32_16x16x128_f8f6f4 v[64:67], v[0:7], v[200:207], v[64:67], v190, v190 op_sel_hi:[0,0,0]
	v_mfma_scale_f32_16x16x128_f8f6f4 v[52:55], v[8:15], v[208:215], v[52:55], v190, v190 op_sel_hi:[0,0,0]
	v_mfma_scale_f32_16x16x128_f8f6f4 v[48:51], v[0:7], v[208:215], v[48:51], v190, v190 op_sel_hi:[0,0,0]
	v_mfma_scale_f32_16x16x128_f8f6f4 v[36:39], v[8:15], v[216:223], v[36:39], v190, v190 op_sel_hi:[0,0,0]
	v_mfma_scale_f32_16x16x128_f8f6f4 v[32:35], v[0:7], v[216:223], v[32:35], v190, v190 op_sel_hi:[0,0,0]
	s_setprio 0
	s_barrier
; #define PG8_STAGE(bufoff, gbase, voff) do { _Pragma("unroll") for (int _i = 0; _i < 2; ++_i) \
;         __builtin_amdgcn_global_load_lds((const unsigned*)((const char*)(gbase) + (voff)[_i]), (PG8_LAS unsigned*)(lds + (bufoff) + ldsw + _i * 8192), 16, 0, 0); } while (0)
; #define PG8_LDA(dst, b, h) do { _Pragma("unroll") for (int m = 0; m < 4; ++m) _Pragma("unroll") for (int k = 0; k < 2; ++k) dst[m][k] = *(const PG8_LAS bf16x8*)(lds + PG8_SA(b, h) + aoff + m * 2048 + k * KFR); } while (0)
; #define PG8_LDB(dst, b, h) do { _Pragma("unroll") for (int n = 0; n < 2; ++n) _Pragma("unroll") for (int k = 0; k < 2; ++k) dst[n][k] = *(const PG8_LAS bf16x8*)(lds + PG8_SB(b, h) + boff + n * 2048 + k * KFR); } while (0)
; #define PG8_WAIT_V(n) asm volatile("s_waitcnt vmcnt(" #n ")" ::: "memory")
; #define PG8_WAIT_L(n) asm volatile("s_waitcnt lgkmcnt(" #n ")" ::: "memory")
; #define PG8_BAR __builtin_amdgcn_s_barrier()
; #define PG8_SCHED __builtin_amdgcn_sched_barrier(0)
; template <class Epi, class Sched, bool ALIGN_EPI = false, bool SP2 = false, bool GATHER = false, bool F8 = false>
; __device__ __forceinline__ void gemm_phase(PG8_LAS unsigned char* lds, const Gemm g, const Sched& S, const Epi& E) {
;     ...
;             PG8_LDB(B0, 1, 0); PG8_LDB(B1, 1, 1); PG8_SCHED; PG8_LDA(At, 1, 0); PG8_STAGE_A(PG8_SA(0, 1), a2, 1, last);
;             PG8_WAIT_V(8); PG8_WAIT_L(0); PG8_BAR; PG8_MMA(0, 0, At, B0); PG8_MMA(0, 1, At, B1); PG8_BAR; PG8_SCHED;
;             PG8_LDA(At, 1, 1); PG8_STAGE(PG8_SB(1, 0), b3, voffB); PG8_STAGE(PG8_SB(1, 1), b3 + hstep, voffB); PG8_STAGE_A(PG8_SA(1, 0), a3, 0, last);
;             PG8_WAIT_V(8); PG8_WAIT_L(0); PG8_BAR; PG8_MMA(1, 0, At, B0); PG8_MMA(1, 1, At, B1); PG8_BAR; PG8_SCHED;
	s_add_i32 s79, 0, 0x18000
	s_add_i32 s80, 0, 0x1c000
	v_add_u32_e32 v12, s79, v185
	v_add_u32_e32 v28, s80, v185
	ds_read_b128 v[0:3], v12
	ds_read_b128 v[4:7], v12 offset:1024
	ds_read_b128 v[8:11], v12 offset:2048
	ds_read_b128 v[12:15], v12 offset:3072
	ds_read_b128 v[16:19], v28
	ds_read_b128 v[20:23], v28 offset:1024
	ds_read_b128 v[24:27], v28 offset:2048
	ds_read_b128 v[28:31], v28 offset:3072
	s_add_u32 s60, s64, 0x40000
	s_addc_u32 s61, s65, 0
	s_mov_b32 m0, s31
	v_lshl_add_u64 v[226:227], s[60:61], 0, v[164:165]
	ds_read_b128 v[192:195], v189 offset:32768
	ds_read_b128 v[196:199], v189 offset:33792
	ds_read_b128 v[200:203], v189 offset:34816
	ds_read_b128 v[204:207], v189 offset:35840
	ds_read_b128 v[208:211], v189 offset:36864
	ds_read_b128 v[212:215], v189 offset:37888
	ds_read_b128 v[216:219], v189 offset:38912
	ds_read_b128 v[220:223], v189 offset:39936
	global_load_lds_dwordx4 v[226:227], off
	v_lshl_add_u64 v[226:227], s[60:61], 0, v[166:167]
	s_mov_b32 m0, s33
	s_nop 0
	global_load_lds_dwordx4 v[226:227], off
	s_waitcnt vmcnt(8)
	s_waitcnt lgkmcnt(0)
	s_barrier
	s_setprio 1
	s_waitcnt lgkmcnt(0)
	v_mfma_scale_f32_16x16x128_f8f6f4 v[156:159], v[0:7], v[192:199], v[156:159], v190, v190 op_sel_hi:[0,0,0]
	v_mfma_scale_f32_16x16x128_f8f6f4 v[152:155], v[8:15], v[192:199], v[152:155], v190, v190 op_sel_hi:[0,0,0]
	v_mfma_scale_f32_16x16x128_f8f6f4 v[148:151], v[0:7], v[200:207], v[148:151], v190, v190 op_sel_hi:[0,0,0]
	v_mfma_scale_f32_16x16x128_f8f6f4 v[144:147], v[8:15], v[200:207], v[144:147], v190, v190 op_sel_hi:[0,0,0]
	v_mfma_scale_f32_16x16x128_f8f6f4 v[124:127], v[0:7], v[208:215], v[124:127], v190, v190 op_sel_hi:[0,0,0]
	v_mfma_scale_f32_16x16x128_f8f6f4 v[120:123], v[8:15], v[208:215], v[120:123], v190, v190 op_sel_hi:[0,0,0]
	v_mfma_scale_f32_16x16x128_f8f6f4 v[108:111], v[0:7], v[216:223], v[108:111], v190, v190 op_sel_hi:[0,0,0]
	v_mfma_scale_f32_16x16x128_f8f6f4 v[104:107], v[8:15], v[216:223], v[104:107], v190, v190 op_sel_hi:[0,0,0]
	s_setprio 0
	s_setprio 1
	v_mfma_scale_f32_16x16x128_f8f6f4 v[140:143], v[16:23], v[192:199], v[140:143], v190, v190 op_sel_hi:[0,0,0]
	v_mfma_scale_f32_16x16x128_f8f6f4 v[136:139], v[24:31], v[192:199], v[136:139], v190, v190 op_sel_hi:[0,0,0]
	v_mfma_scale_f32_16x16x128_f8f6f4 v[132:135], v[16:23], v[200:207], v[132:135], v190, v190 op_sel_hi:[0,0,0]
	v_mfma_scale_f32_16x16x128_f8f6f4 v[128:131], v[24:31], v[200:207], v[128:131], v190, v190 op_sel_hi:[0,0,0]
	v_mfma_scale_f32_16x16x128_f8f6f4 v[116:119], v[16:23], v[208:215], v[116:119], v190, v190 op_sel_hi:[0,0,0]
	v_mfma_scale_f32_16x16x128_f8f6f4 v[112:115], v[24:31], v[208:215], v[112:115], v190, v190 op_sel_hi:[0,0,0]
	v_mfma_scale_f32_16x16x128_f8f6f4 v[100:103], v[16:23], v[216:223], v[100:103], v190, v190 op_sel_hi:[0,0,0]
	v_mfma_scale_f32_16x16x128_f8f6f4 v[96:99], v[24:31], v[216:223], v[96:99], v190, v190 op_sel_hi:[0,0,0]
	s_setprio 0
	s_barrier
	s_add_i32 s60, s79, s26
	v_lshl_add_u64 v[176:177], v[176:177], 0, s[12:13]
	s_mov_b32 m0, s60
	ds_read_b128 v[192:195], v189 offset:49152
	ds_read_b128 v[196:199], v189 offset:50176
	ds_read_b128 v[200:203], v189 offset:51200
	ds_read_b128 v[204:207], v189 offset:52224
	ds_read_b128 v[208:211], v189 offset:53248
	ds_read_b128 v[212:215], v189 offset:54272
	ds_read_b128 v[216:219], v189 offset:55296
	ds_read_b128 v[220:223], v189 offset:56320
	global_load_lds_dwordx4 v[176:177], off
	s_add_i32 m0, s60, 0x2000
	s_add_u32 s60, s62, 0x40080
	v_lshl_add_u64 v[176:177], v[178:179], 0, s[12:13]
	s_addc_u32 s61, s63, 0
	s_add_i32 s62, s80, s26
	global_load_lds_dwordx4 v[176:177], off
	v_lshl_add_u64 v[176:177], s[60:61], 0, v[162:163]
	s_mov_b32 m0, s62
	s_nop 0
	global_load_lds_dwordx4 v[176:177], off
	v_lshl_add_u64 v[176:177], s[60:61], 0, v[168:169]
	s_add_i32 m0, s62, 0x2000
	s_nop 0
	global_load_lds_dwordx4 v[176:177], off
	v_lshl_add_u64 v[176:177], v[180:181], 0, s[12:13]
	s_mov_b32 m0, s66
	s_nop 0
	global_load_lds_dwordx4 v[176:177], off
	v_lshl_add_u64 v[176:177], v[182:183], 0, s[12:13]
	s_mov_b32 m0, s67
	s_nop 0
	global_load_lds_dwordx4 v[176:177], off
	s_waitcnt vmcnt(8)
	s_waitcnt lgkmcnt(0)
	s_barrier
	s_setprio 1
	s_waitcnt lgkmcnt(0)
	v_mfma_scale_f32_16x16x128_f8f6f4 v[92:95], v[0:7], v[192:199], v[92:95], v190, v190 op_sel_hi:[0,0,0]
	v_mfma_scale_f32_16x16x128_f8f6f4 v[88:91], v[8:15], v[192:199], v[88:91], v190, v190 op_sel_hi:[0,0,0]
	v_mfma_scale_f32_16x16x128_f8f6f4 v[76:79], v[0:7], v[200:207], v[76:79], v190, v190 op_sel_hi:[0,0,0]
	v_mfma_scale_f32_16x16x128_f8f6f4 v[72:75], v[8:15], v[200:207], v[72:75], v190, v190 op_sel_hi:[0,0,0]
	v_mfma_scale_f32_16x16x128_f8f6f4 v[60:63], v[0:7], v[208:215], v[60:63], v190, v190 op_sel_hi:[0,0,0]
	v_mfma_scale_f32_16x16x128_f8f6f4 v[56:59], v[8:15], v[208:215], v[56:59], v190, v190 op_sel_hi:[0,0,0]
	v_mfma_scale_f32_16x16x128_f8f6f4 v[44:47], v[0:7], v[216:223], v[44:47], v190, v190 op_sel_hi:[0,0,0]
	v_mfma_scale_f32_16x16x128_f8f6f4 v[40:43], v[8:15], v[216:223], v[40:43], v190, v190 op_sel_hi:[0,0,0]
	s_setprio 0
	s_setprio 1
	v_mfma_scale_f32_16x16x128_f8f6f4 v[84:87], v[16:23], v[192:199], v[84:87], v190, v190 op_sel_hi:[0,0,0]
	v_mfma_scale_f32_16x16x128_f8f6f4 v[80:83], v[24:31], v[192:199], v[80:83], v190, v190 op_sel_hi:[0,0,0]
	v_mfma_scale_f32_16x16x128_f8f6f4 v[68:71], v[16:23], v[200:207], v[68:71], v190, v190 op_sel_hi:[0,0,0]
	v_mfma_scale_f32_16x16x128_f8f6f4 v[64:67], v[24:31], v[200:207], v[64:67], v190, v190 op_sel_hi:[0,0,0]
	v_mfma_scale_f32_16x16x128_f8f6f4 v[52:55], v[16:23], v[208:215], v[52:55], v190, v190 op_sel_hi:[0,0,0]
	v_mfma_scale_f32_16x16x128_f8f6f4 v[48:51], v[24:31], v[208:215], v[48:51], v190, v190 op_sel_hi:[0,0,0]
	v_mfma_scale_f32_16x16x128_f8f6f4 v[36:39], v[16:23], v[216:223], v[36:39], v190, v190 op_sel_hi:[0,0,0]
	v_mfma_scale_f32_16x16x128_f8f6f4 v[32:35], v[24:31], v[216:223], v[32:35], v190, v190 op_sel_hi:[0,0,0]
	s_setprio 0
	s_barrier
	s_add_i32 s78, s78, 2
	s_add_u32 s76, s76, 0x100
	s_addc_u32 s77, s77, 0
	s_cmp_gt_u32 s78, 13
	s_mov_b64 s[60:61], s[58:59]
	s_cbranch_scc0 .LBB0_1565
	s_and_b64 vcc, exec, s[14:15]
	s_cbranch_vccz .LBB0_1568
	s_barrier
